# BN stats rows spread over four 4KB blocks per layer (sum-of-squares rows shifted one slot) to relieve memory-channel hot-spotting
# baseline (speedup 1.0000x reference)
.LBB0_6:
	s_lshr_b32 s12, s2, 3
	s_mov_b32 s13, 0
	s_and_b32 s3, s2, 7
	s_lshl_b64 s[0:1], s[12:13], 20
	v_lshrrev_b32_e32 v62, 6, v0
	v_and_b32_e32 v1, 63, v0
	v_lshlrev_b32_e32 v2, 13, v62
	v_lshlrev_b32_e32 v63, 4, v1
	v_lshl_add_u32 v2, s3, 17, v2
	v_or_b32_e32 v68, v2, v63
	s_mov_b32 s11, 0x20000
	s_mov_b32 s10, 0x100000
	s_waitcnt lgkmcnt(0)
	s_add_u32 s8, s4, s0
	s_addc_u32 s9, s5, s1
	s_and_b32 s9, s9, 0xffff
	v_mov_b32_e32 v46, v68
	buffer_load_dwordx4 v[26:29], v46, s[8:11], 0 offen sc0 nt
	buffer_load_dwordx4 v[10:13], v46, s[8:11], 0 offen offset:1024 sc0 nt
	buffer_load_dwordx4 v[34:37], v46, s[8:11], 0 offen offset:2048 sc0 nt
	buffer_load_dwordx4 v[14:17], v46, s[8:11], 0 offen offset:3072 sc0 nt
	v_add_u32_e32 v47, 0x1000, v46
	buffer_load_dwordx4 v[30:33], v47, s[8:11], 0 offen sc0 nt
	buffer_load_dwordx4 v[18:21], v47, s[8:11], 0 offen offset:1024 sc0 nt
	buffer_load_dwordx4 v[38:41], v47, s[8:11], 0 offen offset:2048 sc0 nt
	buffer_load_dwordx4 v[22:25], v47, s[8:11], 0 offen offset:3072 sc0 nt
	v_add_u32_e32 v46, 0x8000, v68
	buffer_load_dwordx4 v[96:99], v46, s[8:11], 0 offen sc0 nt
	buffer_load_dwordx4 v[80:83], v46, s[8:11], 0 offen offset:1024 sc0 nt
	buffer_load_dwordx4 v[104:107], v46, s[8:11], 0 offen offset:2048 sc0 nt
	buffer_load_dwordx4 v[84:87], v46, s[8:11], 0 offen offset:3072 sc0 nt
	v_add_u32_e32 v47, 0x1000, v46
	buffer_load_dwordx4 v[100:103], v47, s[8:11], 0 offen sc0 nt
	buffer_load_dwordx4 v[88:91], v47, s[8:11], 0 offen offset:1024 sc0 nt
	buffer_load_dwordx4 v[108:111], v47, s[8:11], 0 offen offset:2048 sc0 nt
	buffer_load_dwordx4 v[92:95], v47, s[8:11], 0 offen offset:3072 sc0 nt
	v_mbcnt_lo_u32_b32 v3, -1, 0
	v_mbcnt_hi_u32_b32 v3, -1, v3
	s_lshr_b32 s12, s2, 3
	s_mov_b32 s13, 0
	v_and_b32_e32 v5, 64, v3
	s_and_b32 s3, s2, 7
	s_lshl_b64 s[0:1], s[12:13], 20
	v_xor_b32_e32 v4, 16, v3
	v_add_u32_e32 v5, 64, v5
	s_waitcnt lgkmcnt(0)
	s_add_u32 s8, s4, s0
	v_cmp_lt_i32_e32 vcc, v4, v5
	v_lshrrev_b32_e32 v62, 6, v0
	s_addc_u32 s0, s5, s1
	s_lshl_b32 s12, s12, 9
	v_cndmask_b32_e32 v4, v3, v4, vcc
	s_and_b32 s9, s0, 0xffff
	v_lshlrev_b32_e32 v2, 2, v62
	v_lshlrev_b32_e32 v65, 2, v4
	v_xor_b32_e32 v4, 32, v3
	s_lshl_b64 s[4:5], s[12:13], 2
	v_and_b32_e32 v1, 63, v0
	v_cmp_lt_i32_e32 vcc, v4, v5
	v_lshl_add_u32 v66, s3, 6, v2
	s_add_u32 s4, s6, s4
	v_lshlrev_b32_e32 v2, 13, v62
	v_lshlrev_b32_e32 v63, 4, v1
	v_cndmask_b32_e32 v3, v3, v4, vcc
	v_lshlrev_b32_e32 v42, 2, v66
	v_mov_b32_e32 v43, 0
	s_addc_u32 s5, s7, s5
	v_lshl_add_u32 v2, s3, 17, v2
	s_mov_b32 s11, 0x20000
	s_mov_b32 s10, 0x100000
	v_lshlrev_b32_e32 v64, 2, v3
	v_cmp_eq_u32_e64 s[0:1], 0, v1
	v_lshl_add_u64 v[44:45], s[4:5], 0, v[42:43]
	v_lshrrev_b32_e32 v67, 2, v66
	v_or_b32_e32 v68, v2, v63
	v_mov_b32_e32 v42, v43
	v_mov_b32_e32 v2, v43
	v_mov_b32_e32 v3, v43
	v_mov_b32_e32 v4, v43
	v_mov_b32_e32 v5, v43
	v_mov_b32_e32 v6, v43
	v_mov_b32_e32 v7, v43
	v_mov_b32_e32 v8, v43
	v_mov_b32_e32 v9, v43
	s_sub_u32 s14, s2, 64
	s_cmp_lt_u32 s14, 7
	s_cbranch_scc0 .Lk1_nozero
	v_lshlrev_b32_e32 v69, 4, v0
	s_lshl_b32 s14, s14, 12
	v_add_u32_e32 v69, s14, v69
	v_add_u32_e32 v69, 0x582000, v69
	global_store_dwordx4 v69, v[2:5], s[6:7]

_Z9k2_layer1PKfS0_S0_PfS1_S1_:
	s_load_dwordx8 s[4:11], s[0:1], 0x0
	s_load_dwordx4 s[12:15], s[0:1], 0x20
	s_lshr_b32 s16, s2, 5
	s_and_b32 s17, s2, 31
	s_lshl_b32 s17, s17, 4
	s_movk_i32 s18, 0x500
	v_and_b32_e32 v1, 15, v0
	v_lshrrev_b32_e32 v2, 4, v0
	v_lshl_add_u32 v3, s16, 4, v2
	v_add_u32_e32 v4, s17, v1
	v_lshlrev_b32_e32 v4, 2, v4
	v_lshl_add_u32 v5, v3, 11, v4
	v_add_u32_e32 v6, 0x40000, v5
	v_lshl_add_u32 v7, v3, 14, v4
	v_add_u32_e32 v7, 0x80000, v7
	v_add_u32_e32 v8, 0x1000, v7
	v_add_u32_e32 v9, 0x2000, v7
	v_add_u32_e32 v10, 0x3000, v7
	v_and_b32_e32 v11, 7, v1
	v_lshl_add_u32 v11, v3, 3, v11
	v_lshlrev_b32_e32 v11, 2, v11
	v_and_b32_e32 v12, 8, v1
	v_lshl_add_u32 v11, v12, 9, v11
	v_add_u32_e32 v11, 0x280000, v11
	v_lshrrev_b32_e32 v13, 6, v0
	v_bfe_u32 v14, v0, 4, 2
	v_lshl_add_u32 v15, v13, 4, v1
	v_mul_u32_u24_e32 v16, 20, v15
	v_mad_u32_u24 v16, v14, s18, v16
	v_add_u32_e32 v17, 0x1400, v16
	v_add_u32_e32 v18, 0x2800, v16
	v_add_u32_e32 v19, 0x3c00, v16
	v_lshlrev_b32_e32 v20, 2, v15
	s_lshl_b32 s19, s2, 4
	v_add_u32_e32 v59, s19, v1
	v_lshlrev_b32_e32 v59, 6, v59
	v_lshl_add_u32 v59, v13, 4, v59
	v_lshl_add_u32 v59, v14, 2, v59
	v_lshlrev_b32_e32 v59, 2, v59
	v_and_b32_e32 v90, 3, v1
	v_lshl_add_u32 v90, v14, 2, v90
	v_lshl_add_u32 v90, v13, 4, v90
	s_lshl_b32 s19, s16, 8
	s_and_b32 s20, s2, 1
	s_mul_i32 s20, s20, 0x3000
	s_add_u32 s19, s19, s20
	v_lshl_add_u32 v90, v90, 2, s19
	v_add_u32_e32 v91, 0x1000, v90
	s_waitcnt lgkmcnt(0)
	global_load_dword v24, v5, s[4:5]
	global_load_dword v25, v6, s[4:5]
	global_load_dword v26, v7, s[4:5]
	global_load_dword v27, v7, s[4:5] offset:2048
	global_load_dword v28, v8, s[4:5]
	global_load_dword v29, v8, s[4:5] offset:2048
	global_load_dword v30, v9, s[4:5]
	global_load_dword v31, v9, s[4:5] offset:2048
	global_load_dword v32, v10, s[4:5]
	global_load_dword v33, v10, s[4:5] offset:2048
	global_load_dword v34, v11, s[4:5]
	global_load_dwordx4 v[36:39], v16, s[6:7]
	global_load_dwordx4 v[40:43], v17, s[6:7]
	global_load_dwordx4 v[44:47], v18, s[6:7]
	global_load_dwordx4 v[48:51], v19, s[6:7]
	global_load_dword v52, v16, s[6:7] offset:16
	global_load_dword v53, v17, s[6:7] offset:16
	global_load_dword v54, v18, s[6:7] offset:16
	global_load_dword v55, v19, s[6:7] offset:16
	global_load_dword v56, v20, s[8:9]
	v_lshlrev_b32_e32 v21, 2, v0
	v_and_b32_e32 v22, 63, v0
	v_lshlrev_b32_e32 v22, 2, v22
	v_lshlrev_b32_e32 v23, 2, v14
	v_add_u32_e32 v23, 0xc00, v23
	v_lshlrev_b32_e32 v57, 3, v12
	v_lshl_add_u32 v57, v2, 2, v57
	v_add_u32_e32 v57, 0xc00, v57
	v_mul_u32_u24_e32 v58, 0x900000, v12
	v_sub_u32_e32 v58, 0x3b000000, v58
	v_mov_b32_e32 v89, 1.0
	s_mov_b32 s20, 0x01010101
	s_mov_b32 s21, 0x01010101
	s_mov_b32 s30, 0xaaaaaaaa
	s_mov_b32 s31, 0xaaaaaaaa
	s_mov_b32 s32, 0xcccccccc
	s_mov_b32 s33, 0xcccccccc
	s_mov_b32 s34, 0xf0f0f0f0
	s_mov_b32 s35, 0xf0f0f0f0
	s_mov_b32 s36, 0x000f000f
	s_mov_b32 s37, 0x000f000f
	s_mov_b32 s38, 0x00f000f0
	s_mov_b32 s39, 0x00f000f0
	s_mov_b32 s22, 0xffff
	s_mov_b32 s23, 0
	s_waitcnt vmcnt(9)
	v_add_f32_dpp v34, v34, v34 quad_perm:[1,0,3,2] row_mask:0xf bank_mask:0xf
	v_add_f32_e32 v26, v26, v27
	v_add_f32_e32 v28, v28, v29
	v_add_f32_dpp v34, v34, v34 quad_perm:[2,3,0,1] row_mask:0xf bank_mask:0xf
	v_add_f32_e32 v30, v30, v31
	v_add_f32_e32 v32, v32, v33
	v_add_f32_dpp v34, v34, v34 row_half_mirror row_mask:0xf bank_mask:0xf
	v_add_f32_e32 v26, v26, v28
	v_add_f32_e32 v30, v30, v32
	v_mul_f32_e32 v25, 0x3b000000, v25
	v_add_f32_e32 v26, v26, v30
	v_mul_f32_e32 v34, v58, v34
	v_mul_f32_e32 v26, 0x3b000000, v26
	ds_write_b32 v21, v24
	ds_write_b32 v21, v25 offset:1024
	ds_write_b32 v21, v26 offset:2048
	s_mov_b64 exec, s[20:21]
	ds_write_b32 v57, v34
	s_mov_b64 exec, -1
	s_waitcnt lgkmcnt(0)
	s_barrier
	ds_read2st64_b32 v[60:61], v22 offset0:0 offset1:1
	ds_read2st64_b32 v[62:63], v22 offset0:2 offset1:3
	ds_read2st64_b32 v[64:65], v22 offset0:4 offset1:5
	ds_read2st64_b32 v[66:67], v22 offset0:6 offset1:7
	ds_read2st64_b32 v[68:69], v22 offset0:8 offset1:9
	ds_read2st64_b32 v[70:71], v22 offset0:10 offset1:11
	ds_read2_b32 v[72:73], v23 offset0:0 offset1:16
	ds_read2_b32 v[74:75], v23 offset0:4 offset1:20
	ds_read2_b32 v[76:77], v23 offset0:8 offset1:24
	ds_read2_b32 v[78:79], v23 offset0:12 offset1:28
	s_waitcnt vmcnt(0)
	s_waitcnt lgkmcnt(9)
	v_mfma_f32_16x16x4_f32 v[80:83], v36, v60, 0
	v_mfma_f32_16x16x4_f32 v[84:87], v40, v61, 0
	s_waitcnt lgkmcnt(8)
	v_mfma_f32_16x16x4_f32 v[80:83], v44, v62, v[80:83]
	v_mfma_f32_16x16x4_f32 v[84:87], v48, v63, v[84:87]
	s_waitcnt lgkmcnt(7)
	v_mfma_f32_16x16x4_f32 v[80:83], v38, v64, v[80:83]
	v_mfma_f32_16x16x4_f32 v[84:87], v42, v65, v[84:87]
	v_cndmask_b32_e64 v88, 0, v56, s[22:23]
	s_waitcnt lgkmcnt(6)
	v_mfma_f32_16x16x4_f32 v[80:83], v46, v66, v[80:83]
	v_mfma_f32_16x16x4_f32 v[84:87], v50, v67, v[84:87]
	s_waitcnt lgkmcnt(0)
	v_fmac_f32_e32 v88, v37, v72
	v_fmac_f32_e32 v88, v52, v73
	v_fmac_f32_e32 v88, v41, v74
	v_fmac_f32_e32 v88, v53, v75
	v_fmac_f32_e32 v88, v45, v76
	v_fmac_f32_e32 v88, v54, v77
	v_fmac_f32_e32 v88, v49, v78
	v_fmac_f32_e32 v88, v55, v79
	s_waitcnt lgkmcnt(5)
	v_mfma_f32_16x16x4_f32 v[80:83], v39, v68, v[80:83]
	v_mfma_f32_16x16x4_f32 v[84:87], v43, v69, v[84:87]
	s_waitcnt lgkmcnt(4)
	v_mfma_f32_16x16x4_f32 v[80:83], v47, v70, v[80:83]
	v_mfma_f32_16x16x4_f32 v[84:87], v51, v71, v[84:87]
	v_mfma_f32_16x16x4_f32 v[80:83], v88, v89, v[80:83]
	s_nop 7
	s_nop 1
	v_add_f32_e32 v80, v80, v84
	v_add_f32_e32 v81, v81, v85
	v_add_f32_e32 v82, v82, v86
	v_add_f32_e32 v83, v83, v87
	v_max_f32_e32 v80, 0, v80
	v_max_f32_e32 v81, 0, v81
	v_max_f32_e32 v82, 0, v82
	v_max_f32_e32 v83, 0, v83
	global_store_dwordx4 v59, v[80:83], s[10:11] sc1
	v_mul_f32_e32 v84, v80, v80
	v_mul_f32_e32 v85, v81, v81
	v_mul_f32_e32 v86, v82, v82
	v_mul_f32_e32 v87, v83, v83
	v_add_f32_dpp v80, v80, v80 quad_perm:[1,0,3,2] row_mask:0xf bank_mask:0xf
	v_add_f32_dpp v81, v81, v81 quad_perm:[1,0,3,2] row_mask:0xf bank_mask:0xf
	v_add_f32_dpp v82, v82, v82 quad_perm:[1,0,3,2] row_mask:0xf bank_mask:0xf
	v_add_f32_dpp v83, v83, v83 quad_perm:[1,0,3,2] row_mask:0xf bank_mask:0xf
	v_add_f32_dpp v84, v84, v84 quad_perm:[1,0,3,2] row_mask:0xf bank_mask:0xf
	v_add_f32_dpp v85, v85, v85 quad_perm:[1,0,3,2] row_mask:0xf bank_mask:0xf
	v_add_f32_dpp v86, v86, v86 quad_perm:[1,0,3,2] row_mask:0xf bank_mask:0xf
	v_add_f32_dpp v87, v87, v87 quad_perm:[1,0,3,2] row_mask:0xf bank_mask:0xf
	v_add_f32_dpp v80, v80, v80 quad_perm:[2,3,0,1] row_mask:0xf bank_mask:0xf
	v_add_f32_dpp v81, v81, v81 quad_perm:[2,3,0,1] row_mask:0xf bank_mask:0xf
	v_add_f32_dpp v82, v82, v82 quad_perm:[2,3,0,1] row_mask:0xf bank_mask:0xf
	v_add_f32_dpp v83, v83, v83 quad_perm:[2,3,0,1] row_mask:0xf bank_mask:0xf
	v_add_f32_dpp v84, v84, v84 quad_perm:[2,3,0,1] row_mask:0xf bank_mask:0xf
	v_add_f32_dpp v85, v85, v85 quad_perm:[2,3,0,1] row_mask:0xf bank_mask:0xf
	v_add_f32_dpp v86, v86, v86 quad_perm:[2,3,0,1] row_mask:0xf bank_mask:0xf
	v_add_f32_dpp v87, v87, v87 quad_perm:[2,3,0,1] row_mask:0xf bank_mask:0xf
	v_add_f32_dpp v80, v80, v80 row_half_mirror row_mask:0xf bank_mask:0xf
	v_add_f32_dpp v81, v81, v81 row_half_mirror row_mask:0xf bank_mask:0xf
	v_add_f32_dpp v82, v82, v82 row_half_mirror row_mask:0xf bank_mask:0xf
	v_add_f32_dpp v83, v83, v83 row_half_mirror row_mask:0xf bank_mask:0xf
	v_add_f32_dpp v84, v84, v84 row_half_mirror row_mask:0xf bank_mask:0xf
	v_add_f32_dpp v85, v85, v85 row_half_mirror row_mask:0xf bank_mask:0xf
	v_add_f32_dpp v86, v86, v86 row_half_mirror row_mask:0xf bank_mask:0xf
	v_add_f32_dpp v87, v87, v87 row_half_mirror row_mask:0xf bank_mask:0xf
	v_add_f32_dpp v80, v80, v80 row_mirror row_mask:0xf bank_mask:0xf
	v_add_f32_dpp v81, v81, v81 row_mirror row_mask:0xf bank_mask:0xf
	v_add_f32_dpp v82, v82, v82 row_mirror row_mask:0xf bank_mask:0xf
	v_add_f32_dpp v83, v83, v83 row_mirror row_mask:0xf bank_mask:0xf
	v_add_f32_dpp v84, v84, v84 row_mirror row_mask:0xf bank_mask:0xf
	v_add_f32_dpp v85, v85, v85 row_mirror row_mask:0xf bank_mask:0xf
	v_add_f32_dpp v86, v86, v86 row_mirror row_mask:0xf bank_mask:0xf
	v_add_f32_dpp v87, v87, v87 row_mirror row_mask:0xf bank_mask:0xf
	v_cndmask_b32_e64 v80, v80, v81, s[30:31]
	v_cndmask_b32_e64 v82, v82, v83, s[30:31]
	v_cndmask_b32_e64 v84, v84, v85, s[30:31]
	v_cndmask_b32_e64 v86, v86, v87, s[30:31]
	v_cndmask_b32_e64 v80, v80, v82, s[32:33]
	v_cndmask_b32_e64 v84, v84, v86, s[32:33]
	v_cndmask_b32_e64 v80, v80, v84, s[34:35]
	s_mov_b64 exec, s[36:37]
	global_atomic_add_f32 v90, v80, s[12:13]
	s_mov_b64 exec, s[38:39]
	global_atomic_add_f32 v91, v80, s[14:15]
	s_endpgm

_Z7k_layerPKfS0_S0_S0_S0_S0_S0_PfS1_S1_:
	s_load_dwordx4 s[28:31], s[0:1], 0x40
	s_mov_b32 s36, 0xaaaaaaaa
	s_mov_b32 s37, 0xaaaaaaaa
	s_mov_b32 s38, 0xcccccccc
	s_mov_b32 s39, 0xcccccccc
	s_mov_b32 s40, 0xf0f0f0f0
	s_mov_b32 s41, 0xf0f0f0f0
	s_mov_b32 s42, 0x000f000f
	s_mov_b32 s43, 0x000f000f
	s_mov_b32 s44, 0x00f000f0
	s_mov_b32 s45, 0x00f000f0
	s_load_dwordx2 s[10:11], s[0:1], 0x0
	s_load_dwordx4 s[12:15], s[0:1], 0x28
	s_load_dwordx2 s[8:9], s[0:1], 0x38
	v_cmp_lt_u32_e64 s[6:7], 63, v0
	v_cmp_gt_u32_e64 s[4:5], 64, v0
	v_mov_b32_e32 v70, 0x7fc00000
	v_lshlrev_b32_e32 v18, 2, v0
	s_and_saveexec_b64 s[16:17], s[4:5]
	s_cbranch_execz .LBB2_2
	s_load_dwordx8 s[20:27], s[0:1], 0x8
	s_waitcnt lgkmcnt(0)
	v_add_u32_e32 v77, 0x3000, v18
	v_add_u32_e32 v78, 0x1000, v18
	v_add_u32_e32 v79, 0x1000, v77
	global_load_dword v81, v77, s[20:21] offset:256 sc1
	global_load_dword v80, v79, s[22:23] offset:256 sc1
	global_load_dword v83, v77, s[20:21] offset:512 sc1
	global_load_dword v82, v79, s[22:23] offset:512 sc1
	global_load_dword v85, v77, s[20:21] offset:768 sc1
	global_load_dword v84, v79, s[22:23] offset:768 sc1
	global_load_dword v87, v77, s[20:21] offset:1024 sc1
	global_load_dword v86, v79, s[22:23] offset:1024 sc1
	global_load_dword v89, v77, s[20:21] offset:1280 sc1
	global_load_dword v88, v79, s[22:23] offset:1280 sc1
	global_load_dword v91, v77, s[20:21] offset:1536 sc1
	global_load_dword v90, v79, s[22:23] offset:1536 sc1
	global_load_dword v93, v77, s[20:21] offset:1792 sc1
	global_load_dword v92, v79, s[22:23] offset:1792 sc1
	global_load_dword v95, v77, s[20:21] sc1
	global_load_dword v94, v79, s[22:23] sc1
	global_load_dword v48, v18, s[20:21] sc1
	global_load_dword v1, v78, s[22:23] sc1
	global_load_dword v73, v18, s[20:21] offset:256 sc1
	global_load_dword v72, v78, s[22:23] offset:256 sc1
	global_load_dword v69, v18, s[20:21] offset:512 sc1
	global_load_dword v68, v78, s[22:23] offset:512 sc1
	global_load_dword v67, v18, s[20:21] offset:768 sc1
	global_load_dword v66, v78, s[22:23] offset:768 sc1
	global_load_dword v65, v18, s[20:21] offset:1024 sc1
	global_load_dword v64, v78, s[22:23] offset:1024 sc1
	global_load_dword v63, v18, s[20:21] offset:1280 sc1
	global_load_dword v62, v78, s[22:23] offset:1280 sc1
	global_load_dword v61, v18, s[20:21] offset:1536 sc1
	global_load_dword v60, v78, s[22:23] offset:1536 sc1
	global_load_dword v53, v18, s[20:21] offset:1792 sc1
	global_load_dword v52, v78, s[22:23] offset:1792 sc1
	global_load_dword v49, v18, s[24:25]
	global_load_dword v76, v18, s[26:27]
	s_waitcnt vmcnt(16)
	v_add_f32_e32 v70, 0, v1

.LBB2_4:
	s_or_b64 exec, exec, s[2:3]
	v_lshlrev_b32_e32 v23, 2, v23
	s_waitcnt lgkmcnt(0)
	s_barrier
	s_waitcnt vmcnt(25)
	ds_read_b128 v[60:63], v23 offset:512
	ds_read_b128 v[64:67], v23 offset:528
	v_cmp_eq_u32_e32 vcc, 0, v75
	s_and_b32 s9, s9, 0xffff
	s_mov_b32 s11, 0x20000
	s_waitcnt vmcnt(16) lgkmcnt(1)
	v_mul_f32_e32 v48, v58, v60
	s_waitcnt vmcnt(0)
	v_cndmask_b32_e32 v20, 0, v20, vcc
	s_mov_b32 s10, 0x100000
	v_mfma_f32_16x16x4_f32 a[0:3], v48, v14, 0
	v_mul_f32_e32 v14, v56, v61
	v_cmp_eq_u32_e32 vcc, 0, v19
	s_nop 0
	v_mfma_f32_16x16x4_f32 a[4:7], v14, v15, 0
	v_mul_f32_e32 v14, v54, v62
	s_nop 1
	v_mfma_f32_16x16x4_f32 a[0:3], v14, v16, a[0:3]
	v_mul_f32_e32 v14, v50, v63
	s_nop 1
	v_mfma_f32_16x16x4_f32 a[4:7], v14, v17, a[4:7]
	s_waitcnt lgkmcnt(0)
	v_mul_f32_e32 v14, v46, v64
	s_nop 1
	v_mfma_f32_16x16x4_f32 a[0:3], v14, v10, a[0:3]
	v_mul_f32_e32 v10, v44, v65
	ds_read_b128 v[14:17], v23 offset:1024
	ds_read_b128 v[60:63], v23 offset:768
	ds_read_b128 v[68:71], v23 offset:1040
	ds_read_b128 v[76:79], v23 offset:784
	v_mfma_f32_16x16x4_f32 a[4:7], v10, v11, a[4:7]
	v_mul_f32_e32 v11, v42, v66
	s_waitcnt lgkmcnt(3)
	v_mul_f32_e32 v10, v59, v14
	s_waitcnt lgkmcnt(2)
	v_fmac_f32_e32 v10, v58, v60
	v_mul_f32_e32 v14, v57, v15
	v_add_f32_e32 v10, v20, v10
	v_fmac_f32_e32 v14, v56, v61
	v_add_f32_e32 v10, v14, v10
	v_mfma_f32_16x16x4_f32 a[0:3], v11, v12, a[0:3]
	v_mul_f32_e32 v11, v55, v16
	v_mul_f32_e32 v12, v36, v67
	v_fmac_f32_e32 v11, v54, v62
	ds_read_b128 v[52:55], v23 offset:544
	v_add_f32_e32 v14, v11, v10
	v_mul_f32_e32 v15, v51, v17
	v_fmac_f32_e32 v15, v50, v63
	v_mfma_f32_16x16x4_f32 a[4:7], v12, v13, a[4:7]
	ds_read_b128 v[10:13], v23 offset:560
	s_waitcnt lgkmcnt(1)
	v_mul_f32_e32 v16, v40, v52
	v_add_f32_e32 v14, v15, v14
	v_mul_f32_e32 v15, v47, v68
	v_fmac_f32_e32 v15, v46, v76
	v_add_f32_e32 v14, v14, v15
	v_mul_f32_e32 v15, v38, v53
	v_mfma_f32_16x16x4_f32 a[0:3], v16, v6, a[0:3]
	v_mul_f32_e32 v20, v34, v54
	v_mul_f32_e32 v6, v45, v69
	v_fmac_f32_e32 v6, v44, v77
	v_add_f32_e32 v6, v6, v14
	v_mul_f32_e32 v14, v43, v70
	v_fmac_f32_e32 v14, v42, v78
	v_add_f32_e32 v6, v14, v6
	v_mfma_f32_16x16x4_f32 a[4:7], v15, v7, a[4:7]
	ds_read_b128 v[14:17], v23 offset:800
	ds_read_b128 v[42:45], v23 offset:1056
	v_mul_f32_e32 v7, v37, v71
	v_fmac_f32_e32 v7, v36, v79
	v_add_f32_e32 v48, v7, v6
	v_mov_b32_e32 v6, v40
	v_mov_b32_e32 v40, v41
	v_mov_b32_e32 v41, v39
	v_mfma_f32_16x16x4_f32 a[0:3], v20, v8, a[0:3]
	v_mul_f32_e32 v8, v32, v55
	v_mov_b32_e32 v7, v38
	s_waitcnt lgkmcnt(0)
	v_mul_f32_e64 v46, v40, v42
	v_mul_f32_e64 v47, v41, v43
	v_mul_f32_e32 v11, v28, v11
	v_pk_fma_f32 v[6:7], v[6:7], v[14:15], v[46:47]
	ds_read_b128 v[36:39], v23 offset:1072
	ds_read_b128 v[40:43], v23 offset:816
	v_mfma_f32_16x16x4_f32 a[4:7], v8, v9, a[4:7]
	v_mul_f32_e32 v8, v30, v10
	v_add_f32_e32 v6, v48, v6
	v_add_f32_e32 v10, v7, v6
	v_mov_b32_e32 v7, v32
	v_mov_b32_e32 v32, v35
	v_mov_b32_e32 v6, v34
	v_mov_b32_e32 v23, v21
	v_mfma_f32_16x16x4_f32 a[0:3], v8, v2, a[0:3]
	v_mul_f32_e64 v8, v32, v44
	v_mul_f32_e64 v9, v33, v45
	v_mov_b32_e32 v20, 0
	v_fma_f32 v6, v6, v16, v8
	v_fma_f32 v7, v7, v17, v9
	v_mul_f32_e32 v9, v24, v12
	v_add_f32_e32 v2, v6, v10
	v_add_f32_e32 v8, v7, v2
	v_mov_b32_e32 v2, v30
	v_mfma_f32_16x16x4_f32 a[4:7], v11, v3, a[4:7]
	v_mov_b32_e32 v3, v28
	v_mov_b32_e32 v28, v31
	s_waitcnt lgkmcnt(1)
	v_mul_f32_e64 v6, v28, v36
	v_mul_f32_e64 v7, v29, v37
	v_mov_b32_e32 v16, v21
	s_waitcnt lgkmcnt(0)
	v_pk_fma_f32 v[2:3], v[2:3], v[40:41], v[6:7]
	v_mov_b32_e32 v17, v21
	v_add_f32_e32 v2, v8, v2
	v_mfma_f32_16x16x4_f32 a[0:3], v9, v4, a[0:3]
	v_add_f32_e32 v4, v3, v2
	v_mul_f32_e32 v8, v26, v13
	v_mov_b32_e32 v3, v26
	v_mov_b32_e32 v26, v25
	v_mov_b32_e32 v2, v24
	v_pk_mul_f32 v[6:7], v[26:27], v[38:39]
	v_mov_b32_e32 v9, v21
	v_pk_fma_f32 v[2:3], v[2:3], v[42:43], v[6:7]
	v_mfma_f32_16x16x4_f32 a[4:7], v8, v5, a[4:7]
	v_add_f32_e32 v2, v2, v4
	v_add_f32_e32 v4, v3, v2
	v_mov_b32_e32 v5, 1.0
	v_mov_b32_e32 v8, v21
	s_nop 0
	v_mfma_f32_16x16x4_f32 a[0:3], v4, v5, a[0:3]
	s_nop 3
	v_accvgpr_read_b32 v3, a7
	v_accvgpr_read_b32 v2, a6
	v_accvgpr_read_b32 v7, a5
	v_accvgpr_read_b32 v6, a4
	s_nop 1
	v_accvgpr_read_b32 v5, a3
	v_accvgpr_read_b32 v4, a2
	v_pk_add_f32 v[2:3], v[2:3], v[4:5]
	v_accvgpr_read_b32 v5, a1
	v_accvgpr_read_b32 v4, a0
	v_pk_add_f32 v[4:5], v[6:7], v[4:5]
	v_max_f32_e32 v14, 0, v2
	v_max_f32_e32 v12, 0, v4
	v_max_f32_e32 v13, 0, v5
	v_max_f32_e32 v15, 0, v3
	v_lshlrev_b32_e32 v2, 6, v22
	v_and_b32_e32 v3, 12, v1
	v_or3_b32 v2, v2, v74, v3
	v_lshlrev_b32_e32 v2, 2, v2
	buffer_store_dwordx4 v[12:15], v2, s[8:11], 0 offen sc1
	v_mul_f32_e32 v4, v12, v12
	v_mul_f32_e32 v5, v13, v13
	v_mul_f32_e32 v6, v14, v14
	v_mul_f32_e32 v7, v15, v15
	v_and_b32_e32 v8, 3, v19
	v_and_b32_e32 v9, 12, v1
	v_or3_b32 v8, v8, v9, v74
	s_lshl_b32 s2, s12, 8
	s_bfe_u32 s3, s16, 0x10004
	s_mul_i32 s3, s3, 0x3000
	s_add_u32 s2, s2, s3
	v_lshl_add_u32 v8, v8, 2, s2
	v_add_u32_e32 v9, 0x1000, v8
	v_add_f32_dpp v12, v12, v12 quad_perm:[1,0,3,2] row_mask:0xf bank_mask:0xf
	v_add_f32_dpp v13, v13, v13 quad_perm:[1,0,3,2] row_mask:0xf bank_mask:0xf
	v_add_f32_dpp v14, v14, v14 quad_perm:[1,0,3,2] row_mask:0xf bank_mask:0xf
	v_add_f32_dpp v15, v15, v15 quad_perm:[1,0,3,2] row_mask:0xf bank_mask:0xf
	v_add_f32_dpp v4, v4, v4 quad_perm:[1,0,3,2] row_mask:0xf bank_mask:0xf
	v_add_f32_dpp v5, v5, v5 quad_perm:[1,0,3,2] row_mask:0xf bank_mask:0xf
	v_add_f32_dpp v6, v6, v6 quad_perm:[1,0,3,2] row_mask:0xf bank_mask:0xf
	v_add_f32_dpp v7, v7, v7 quad_perm:[1,0,3,2] row_mask:0xf bank_mask:0xf
	v_add_f32_dpp v12, v12, v12 quad_perm:[2,3,0,1] row_mask:0xf bank_mask:0xf
	v_add_f32_dpp v13, v13, v13 quad_perm:[2,3,0,1] row_mask:0xf bank_mask:0xf
	v_add_f32_dpp v14, v14, v14 quad_perm:[2,3,0,1] row_mask:0xf bank_mask:0xf
	v_add_f32_dpp v15, v15, v15 quad_perm:[2,3,0,1] row_mask:0xf bank_mask:0xf
	v_add_f32_dpp v4, v4, v4 quad_perm:[2,3,0,1] row_mask:0xf bank_mask:0xf
	v_add_f32_dpp v5, v5, v5 quad_perm:[2,3,0,1] row_mask:0xf bank_mask:0xf
	v_add_f32_dpp v6, v6, v6 quad_perm:[2,3,0,1] row_mask:0xf bank_mask:0xf
	v_add_f32_dpp v7, v7, v7 quad_perm:[2,3,0,1] row_mask:0xf bank_mask:0xf
	v_add_f32_dpp v12, v12, v12 row_half_mirror row_mask:0xf bank_mask:0xf
	v_add_f32_dpp v13, v13, v13 row_half_mirror row_mask:0xf bank_mask:0xf
	v_add_f32_dpp v14, v14, v14 row_half_mirror row_mask:0xf bank_mask:0xf
	v_add_f32_dpp v15, v15, v15 row_half_mirror row_mask:0xf bank_mask:0xf
	v_add_f32_dpp v4, v4, v4 row_half_mirror row_mask:0xf bank_mask:0xf
	v_add_f32_dpp v5, v5, v5 row_half_mirror row_mask:0xf bank_mask:0xf
	v_add_f32_dpp v6, v6, v6 row_half_mirror row_mask:0xf bank_mask:0xf
	v_add_f32_dpp v7, v7, v7 row_half_mirror row_mask:0xf bank_mask:0xf
	v_add_f32_dpp v12, v12, v12 row_mirror row_mask:0xf bank_mask:0xf
	v_add_f32_dpp v13, v13, v13 row_mirror row_mask:0xf bank_mask:0xf
	v_add_f32_dpp v14, v14, v14 row_mirror row_mask:0xf bank_mask:0xf
	v_add_f32_dpp v15, v15, v15 row_mirror row_mask:0xf bank_mask:0xf
	v_add_f32_dpp v4, v4, v4 row_mirror row_mask:0xf bank_mask:0xf
	v_add_f32_dpp v5, v5, v5 row_mirror row_mask:0xf bank_mask:0xf
	v_add_f32_dpp v6, v6, v6 row_mirror row_mask:0xf bank_mask:0xf
	v_add_f32_dpp v7, v7, v7 row_mirror row_mask:0xf bank_mask:0xf
	v_cndmask_b32_e64 v12, v12, v13, s[36:37]
	v_cndmask_b32_e64 v14, v14, v15, s[36:37]
	v_cndmask_b32_e64 v4, v4, v5, s[36:37]
	v_cndmask_b32_e64 v6, v6, v7, s[36:37]
	v_cndmask_b32_e64 v12, v12, v14, s[38:39]
	v_cndmask_b32_e64 v4, v4, v6, s[38:39]
	v_cndmask_b32_e64 v12, v12, v4, s[40:41]
	s_mov_b64 exec, s[42:43]
	global_atomic_add_f32 v8, v12, s[28:29]
	s_mov_b64 exec, s[44:45]
	global_atomic_add_f32 v9, v12, s[30:31]
	s_endpgm

_Z8k5_finalPKfS0_S0_S0_S0_S0_S0_S0_S0_Pf:
	s_load_dwordx8 s[4:11], s[0:1], 0x28
	s_load_dwordx2 s[12:13], s[0:1], 0x0
	s_load_dwordx8 s[16:23], s[0:1], 0x8
	v_lshrrev_b32_e32 v63, 4, v0
	v_lshlrev_b32_e32 v63, 2, v63
	v_cmp_gt_u32_e32 vcc, 64, v0
	v_mov_b32_e32 v54, 0x7fc00000
	v_lshlrev_b32_e32 v58, 2, v0
	v_mov_b32_e32 v55, 0x7fc00000
	s_waitcnt lgkmcnt(0)
	global_load_dword v63, v63, s[10:11]
	s_and_saveexec_b64 s[14:15], vcc
	s_cbranch_execz .LBB3_2
	v_add_u32_e32 v64, 0x3000, v58
	v_add_u32_e32 v82, 0x1000, v58
	v_add_u32_e32 v83, 0x1000, v64
	global_load_dword v67, v64, s[16:17] sc1
	global_load_dword v66, v83, s[18:19] sc1
	global_load_dword v69, v64, s[16:17] offset:256 sc1
	global_load_dword v68, v83, s[18:19] offset:256 sc1
	global_load_dword v71, v64, s[16:17] offset:512 sc1
	global_load_dword v70, v83, s[18:19] offset:512 sc1
	global_load_dword v73, v64, s[16:17] offset:768 sc1
	global_load_dword v72, v83, s[18:19] offset:768 sc1
	global_load_dword v75, v64, s[16:17] offset:1024 sc1
	global_load_dword v74, v83, s[18:19] offset:1024 sc1
	global_load_dword v77, v64, s[16:17] offset:1280 sc1
	global_load_dword v76, v83, s[18:19] offset:1280 sc1
	global_load_dword v79, v64, s[16:17] offset:1536 sc1
	global_load_dword v78, v83, s[18:19] offset:1536 sc1
	global_load_dword v81, v64, s[16:17] offset:1792 sc1
	global_load_dword v80, v83, s[18:19] offset:1792 sc1
	global_load_dword v3, v58, s[16:17] sc1
	global_load_dword v2, v82, s[18:19] sc1
	global_load_dword v53, v58, s[16:17] offset:256 sc1
	global_load_dword v52, v82, s[18:19] offset:256 sc1
	global_load_dword v51, v58, s[16:17] offset:512 sc1
	global_load_dword v50, v82, s[18:19] offset:512 sc1
	global_load_dword v49, v58, s[16:17] offset:768 sc1
	global_load_dword v48, v82, s[18:19] offset:768 sc1
	global_load_dword v47, v58, s[16:17] offset:1024 sc1
	global_load_dword v46, v82, s[18:19] offset:1024 sc1
	global_load_dword v45, v58, s[16:17] offset:1280 sc1
	global_load_dword v44, v82, s[18:19] offset:1280 sc1
	global_load_dword v43, v58, s[16:17] offset:1536 sc1
	global_load_dword v42, v82, s[18:19] offset:1536 sc1
	global_load_dword v41, v58, s[16:17] offset:1792 sc1
	global_load_dword v40, v82, s[18:19] offset:1792 sc1
	global_load_dword v61, v58, s[20:21]
	global_load_dword v60, v58, s[22:23]
	s_waitcnt vmcnt(16)
	v_pk_add_f32 v[54:55], v[2:3], 0 op_sel_hi:[1,0]
